# W12 + up-proj epilogue: the 8 per-row scale LDS reads issued together at epilogue start (one lgkmcnt wait instead of 8), wait-state padding kept after stores
# baseline (speedup 1.0000x reference)
.LBB0_1176:
	s_mov_b32 s0, -1
	s_lshl_b32 s1, s75, 10
	v_mbcnt_lo_u32_b32 v108, s0, 0
	v_mbcnt_hi_u32_b32 v108, s0, v108
	v_lshrrev_b32_e32 v162, 1, v108
	v_and_b32_e32 v158, 56, v162
	s_add_i32 s4, s71, s1
	v_and_b32_e32 v161, 15, v108
	v_lshl_add_u32 v108, v158, 2, s4
	s_lshl_b32 s4, s74, 8
	s_lshl_b32 s0, s44, 8
	s_add_i32 s1, s72, s1
	s_or_b32 s4, s4, s61
	s_add_i32 s0, s0, s60
	v_add_u32_e32 v163, s4, v158
	v_lshl_add_u32 v158, v161, 2, s1
	v_and_b32_e32 v162, 24, v162
	v_or_b32_e32 v160, s0, v161
	ds_read_b128 v[124:127], v108
	ds_read_b128 v[120:123], v108 offset:16
	ds_read_b128 v[112:115], v108 offset:512
	ds_read_b128 v[108:111], v108 offset:528
	v_lshl_or_b32 v161, v161, 5, v162
	ds_read_b32 v162, v158
	ds_read_b32 v166, v158 offset:64
	ds_read_b32 v168, v158 offset:128
	ds_read_b32 v170, v158 offset:192
	ds_read_b32 v172, v158 offset:512
	ds_read_b32 v174, v158 offset:576
	ds_read_b32 v176, v158 offset:640
	ds_read_b32 v178, v158 offset:704
	s_ashr_i32 s0, s0, 8
	s_ashr_i32 s1, s0, 31
	s_lshl_b64 s[0:1], s[0:1], 7
	v_bfe_u32 v159, v163, 5, 1
	s_waitcnt lgkmcnt(0)
	v_pk_fma_f32 v[142:143], v[142:143], v[162:163], v[126:127] op_sel_hi:[1,0,1]
	v_pk_fma_f32 v[140:141], v[140:141], v[162:163], v[124:125] op_sel_hi:[1,0,1]
	v_pk_fma_f32 v[136:137], v[136:137], v[162:163], v[120:121] op_sel_hi:[1,0,1]
	v_max_f32_e32 v141, 0, v141
	v_max_f32_e32 v140, 0, v140
	v_max_f32_e32 v143, 0, v143
	v_max_f32_e32 v142, 0, v142
	v_max_f32_e32 v137, 0, v137
	v_max_f32_e32 v136, 0, v136
	v_pk_fma_f32 v[138:139], v[138:139], v[162:163], v[122:123] op_sel_hi:[1,0,1]
	v_pk_mul_f32 v[142:143], v[142:143], v[142:143]
	v_pk_mul_f32 v[140:141], v[140:141], v[140:141]
	v_pk_mul_f32 v[136:137], v[136:137], v[136:137]
	v_max_f32_e32 v139, 0, v139
	v_max_f32_e32 v138, 0, v138
	v_cvt_pk_bf16_f32 v140, v140, v141
	v_cvt_pk_bf16_f32 v141, v142, v143
	v_cvt_pk_bf16_f32 v142, v136, v137
	v_ashrrev_i32_e32 v136, 6, v163
	v_pk_mul_f32 v[138:139], v[138:139], v[138:139]
	v_ashrrev_i32_e32 v137, 31, v136
	v_cvt_pk_bf16_f32 v143, v138, v139
	v_lshl_add_u64 v[138:139], s[0:1], 0, v[136:137]
	v_or_b32_e32 v164, s70, v159
	v_lshlrev_b64 v[138:139], 15, v[138:139]
	v_lshlrev_b32_e32 v161, 1, v161
	v_pk_fma_f32 v[134:135], v[134:135], v[162:163], v[114:115] op_sel_hi:[1,0,1]
	v_pk_fma_f32 v[132:133], v[132:133], v[162:163], v[112:113] op_sel_hi:[1,0,1]
	v_pk_fma_f32 v[128:129], v[128:129], v[162:163], v[108:109] op_sel_hi:[1,0,1]
	v_lshl_add_u64 v[138:139], s[22:23], 0, v[138:139]
	v_lshl_or_b32 v212, v164, 10, v161
	v_max_f32_e32 v133, 0, v133
	v_max_f32_e32 v132, 0, v132
	v_max_f32_e32 v135, 0, v135
	v_max_f32_e32 v134, 0, v134
	v_max_f32_e32 v129, 0, v129
	v_max_f32_e32 v128, 0, v128
	v_lshl_add_u64 v[164:165], v[138:139], 0, v[212:213]
	v_pk_mul_f32 v[134:135], v[134:135], v[134:135]
	v_pk_mul_f32 v[132:133], v[132:133], v[132:133]
	v_pk_mul_f32 v[128:129], v[128:129], v[128:129]
	global_store_dwordx4 v[164:165], v[140:143], off nt
	v_pk_fma_f32 v[130:131], v[130:131], v[162:163], v[110:111] op_sel_hi:[1,0,1]
	v_cvt_pk_bf16_f32 v132, v132, v133
	v_cvt_pk_bf16_f32 v133, v134, v135
	v_cvt_pk_bf16_f32 v134, v128, v129
	v_add_u32_e32 v128, 0x80, v163
	v_max_f32_e32 v131, 0, v131
	v_max_f32_e32 v130, 0, v130
	v_ashrrev_i32_e32 v128, 6, v128
	v_pk_mul_f32 v[130:131], v[130:131], v[130:131]
	v_ashrrev_i32_e32 v129, 31, v128
	v_cvt_pk_bf16_f32 v135, v130, v131
	v_lshl_add_u64 v[130:131], s[0:1], 0, v[128:129]
	v_lshlrev_b64 v[130:131], 15, v[130:131]
	v_lshl_add_u64 v[130:131], s[22:23], 0, v[130:131]
	v_lshl_add_u64 v[140:141], v[130:131], 0, v[212:213]
	global_store_dwordx4 v[140:141], v[132:135], off nt
	s_nop 0
	s_mov_b64 s[0:1], -1
	s_andn2_b64 vcc, exec, s[36:37]
	s_nop 0
	v_pk_fma_f32 v[118:119], v[118:119], v[166:167], v[126:127] op_sel_hi:[1,0,1]
	v_pk_fma_f32 v[116:117], v[116:117], v[166:167], v[124:125] op_sel_hi:[1,0,1]
	v_pk_fma_f32 v[106:107], v[106:107], v[166:167], v[122:123] op_sel_hi:[1,0,1]
	v_pk_fma_f32 v[104:105], v[104:105], v[166:167], v[120:121] op_sel_hi:[1,0,1]
	v_max_f32_e32 v117, 0, v117
	v_max_f32_e32 v116, 0, v116
	v_max_f32_e32 v119, 0, v119
	v_max_f32_e32 v118, 0, v118
	v_max_f32_e32 v105, 0, v105
	v_max_f32_e32 v104, 0, v104
	v_max_f32_e32 v107, 0, v107
	v_max_f32_e32 v106, 0, v106
	v_pk_fma_f32 v[100:101], v[100:101], v[166:167], v[112:113] op_sel_hi:[1,0,1]
	v_pk_fma_f32 v[98:99], v[98:99], v[166:167], v[110:111] op_sel_hi:[1,0,1]
	v_pk_fma_f32 v[96:97], v[96:97], v[166:167], v[108:109] op_sel_hi:[1,0,1]
	v_pk_mul_f32 v[118:119], v[118:119], v[118:119]
	v_pk_mul_f32 v[116:117], v[116:117], v[116:117]
	v_pk_mul_f32 v[134:135], v[106:107], v[106:107]
	v_pk_mul_f32 v[106:107], v[104:105], v[104:105]
	v_cvt_pk_bf16_f32 v104, v116, v117
	v_cvt_pk_bf16_f32 v105, v118, v119
	v_pk_fma_f32 v[102:103], v[102:103], v[166:167], v[114:115] op_sel_hi:[1,0,1]
	v_max_f32_e32 v101, 0, v101
	v_max_f32_e32 v100, 0, v100
	v_max_f32_e32 v97, 0, v97
	v_max_f32_e32 v96, 0, v96
	v_max_f32_e32 v99, 0, v99
	v_max_f32_e32 v98, 0, v98
	v_cvt_pk_bf16_f32 v106, v106, v107
	v_cvt_pk_bf16_f32 v107, v134, v135
	global_store_dwordx4 v[164:165], v[104:107], off offset:2048 nt
	v_max_f32_e32 v103, 0, v103
	v_max_f32_e32 v102, 0, v102
	v_pk_mul_f32 v[100:101], v[100:101], v[100:101]
	v_pk_mul_f32 v[104:105], v[98:99], v[98:99]
	v_pk_mul_f32 v[98:99], v[96:97], v[96:97]
	v_cvt_pk_bf16_f32 v96, v100, v101
	v_pk_mul_f32 v[102:103], v[102:103], v[102:103]
	s_nop 0
	v_cvt_pk_bf16_f32 v97, v102, v103
	v_cvt_pk_bf16_f32 v98, v98, v99
	v_cvt_pk_bf16_f32 v99, v104, v105
	global_store_dwordx4 v[140:141], v[96:99], off offset:2048 nt
	s_nop 0
	s_nop 0
	v_pk_fma_f32 v[92:93], v[92:93], v[168:169], v[124:125] op_sel_hi:[1,0,1]
	v_pk_fma_f32 v[94:95], v[94:95], v[168:169], v[126:127] op_sel_hi:[1,0,1]
	v_pk_fma_f32 v[90:91], v[90:91], v[168:169], v[122:123] op_sel_hi:[1,0,1]
	v_pk_fma_f32 v[88:89], v[88:89], v[168:169], v[120:121] op_sel_hi:[1,0,1]
	v_max_f32_e32 v93, 0, v93
	v_max_f32_e32 v92, 0, v92
	v_max_f32_e32 v95, 0, v95
	v_max_f32_e32 v94, 0, v94
	v_max_f32_e32 v89, 0, v89
	v_max_f32_e32 v88, 0, v88
	v_max_f32_e32 v91, 0, v91
	v_max_f32_e32 v90, 0, v90
	v_pk_mul_f32 v[92:93], v[92:93], v[92:93]
	v_pk_fma_f32 v[84:85], v[84:85], v[168:169], v[112:113] op_sel_hi:[1,0,1]
	v_pk_mul_f32 v[94:95], v[94:95], v[94:95]
	v_pk_mul_f32 v[98:99], v[90:91], v[90:91]
	v_pk_mul_f32 v[90:91], v[88:89], v[88:89]
	v_cvt_pk_bf16_f32 v88, v92, v93
	v_or_b32_e32 v92, 0x1000, v212
	v_mov_b32_e32 v93, v213
	v_pk_fma_f32 v[82:83], v[82:83], v[168:169], v[110:111] op_sel_hi:[1,0,1]
	v_pk_fma_f32 v[80:81], v[80:81], v[168:169], v[108:109] op_sel_hi:[1,0,1]
	v_max_f32_e32 v85, 0, v85
	v_max_f32_e32 v84, 0, v84
	v_cvt_pk_bf16_f32 v89, v94, v95
	v_lshl_add_u64 v[94:95], v[138:139], 0, v[92:93]
	v_pk_fma_f32 v[86:87], v[86:87], v[168:169], v[114:115] op_sel_hi:[1,0,1]
	v_max_f32_e32 v81, 0, v81
	v_max_f32_e32 v80, 0, v80
	v_max_f32_e32 v83, 0, v83
	v_max_f32_e32 v82, 0, v82
	v_pk_mul_f32 v[84:85], v[84:85], v[84:85]
	v_cvt_pk_bf16_f32 v90, v90, v91
	v_cvt_pk_bf16_f32 v91, v98, v99
	global_store_dwordx4 v[94:95], v[88:91], off nt
	v_max_f32_e32 v87, 0, v87
	v_max_f32_e32 v86, 0, v86
	v_pk_mul_f32 v[88:89], v[82:83], v[82:83]
	v_pk_mul_f32 v[82:83], v[80:81], v[80:81]
	v_cvt_pk_bf16_f32 v80, v84, v85
	v_lshl_add_u64 v[84:85], v[130:131], 0, v[92:93]
	v_pk_mul_f32 v[86:87], v[86:87], v[86:87]
	v_or_b32_e32 v212, 0x1800, v212
	v_cvt_pk_bf16_f32 v81, v86, v87
	v_cvt_pk_bf16_f32 v82, v82, v83
	v_cvt_pk_bf16_f32 v83, v88, v89
	global_store_dwordx4 v[84:85], v[80:83], off nt
	s_nop 0
	s_nop 0
	v_pk_fma_f32 v[76:77], v[76:77], v[170:171], v[124:125] op_sel_hi:[1,0,1]
	v_pk_fma_f32 v[78:79], v[78:79], v[170:171], v[126:127] op_sel_hi:[1,0,1]
	v_pk_fma_f32 v[74:75], v[74:75], v[170:171], v[122:123] op_sel_hi:[1,0,1]
	v_pk_fma_f32 v[72:73], v[72:73], v[170:171], v[120:121] op_sel_hi:[1,0,1]
	v_max_f32_e32 v77, 0, v77
	v_max_f32_e32 v76, 0, v76
	v_max_f32_e32 v79, 0, v79
	v_max_f32_e32 v78, 0, v78
	v_max_f32_e32 v73, 0, v73
	v_max_f32_e32 v72, 0, v72
	v_max_f32_e32 v75, 0, v75
	v_max_f32_e32 v74, 0, v74
	v_pk_mul_f32 v[76:77], v[76:77], v[76:77]
	v_pk_fma_f32 v[68:69], v[68:69], v[170:171], v[112:113] op_sel_hi:[1,0,1]
	v_pk_fma_f32 v[66:67], v[66:67], v[170:171], v[110:111] op_sel_hi:[1,0,1]
	v_pk_fma_f32 v[64:65], v[64:65], v[170:171], v[108:109] op_sel_hi:[1,0,1]
	v_pk_mul_f32 v[78:79], v[78:79], v[78:79]
	v_pk_mul_f32 v[82:83], v[74:75], v[74:75]
	v_pk_mul_f32 v[74:75], v[72:73], v[72:73]
	v_cvt_pk_bf16_f32 v72, v76, v77
	v_cvt_pk_bf16_f32 v73, v78, v79
	v_lshl_add_u64 v[76:77], v[138:139], 0, v[212:213]
	v_pk_fma_f32 v[70:71], v[70:71], v[170:171], v[114:115] op_sel_hi:[1,0,1]
	v_max_f32_e32 v69, 0, v69
	v_max_f32_e32 v68, 0, v68
	v_max_f32_e32 v65, 0, v65
	v_max_f32_e32 v64, 0, v64
	v_max_f32_e32 v67, 0, v67
	v_max_f32_e32 v66, 0, v66
	v_cvt_pk_bf16_f32 v74, v74, v75
	v_cvt_pk_bf16_f32 v75, v82, v83
	global_store_dwordx4 v[76:77], v[72:75], off nt
	v_max_f32_e32 v71, 0, v71
	v_max_f32_e32 v70, 0, v70
	v_pk_mul_f32 v[68:69], v[68:69], v[68:69]
	v_pk_mul_f32 v[72:73], v[66:67], v[66:67]
	v_pk_mul_f32 v[66:67], v[64:65], v[64:65]
	v_pk_mul_f32 v[70:71], v[70:71], v[70:71]
	v_cvt_pk_bf16_f32 v64, v68, v69
	v_lshl_add_u64 v[68:69], v[130:131], 0, v[212:213]
	v_cvt_pk_bf16_f32 v65, v70, v71
	v_cvt_pk_bf16_f32 v66, v66, v67
	v_cvt_pk_bf16_f32 v67, v72, v73
	global_store_dwordx4 v[68:69], v[64:67], off nt
	s_nop 0
	s_nop 0
	v_add_u32_e32 v67, 0x80, v160
	v_ashrrev_i32_e32 v64, 8, v67
	v_lshrrev_b32_e32 v67, 3, v67
	v_and_or_b32 v67, v67, 24, v159
	s_nop 0
	v_pk_fma_f32 v[62:63], v[62:63], v[172:173], v[126:127] op_sel_hi:[1,0,1]
	v_pk_fma_f32 v[60:61], v[60:61], v[172:173], v[124:125] op_sel_hi:[1,0,1]
	v_pk_fma_f32 v[58:59], v[58:59], v[172:173], v[122:123] op_sel_hi:[1,0,1]
	v_pk_fma_f32 v[56:57], v[56:57], v[172:173], v[120:121] op_sel_hi:[1,0,1]
	v_max_f32_e32 v63, 0, v63
	v_max_f32_e32 v62, 0, v62
	v_ashrrev_i32_e32 v65, 31, v64
	v_max_f32_e32 v61, 0, v61
	v_max_f32_e32 v60, 0, v60
	v_max_f32_e32 v57, 0, v57
	v_max_f32_e32 v56, 0, v56
	v_max_f32_e32 v59, 0, v59
	v_max_f32_e32 v58, 0, v58
	v_pk_mul_f32 v[62:63], v[62:63], v[62:63]
	v_pk_mul_f32 v[60:61], v[60:61], v[60:61]
	v_pk_mul_f32 v[68:69], v[58:59], v[58:59]
	v_pk_mul_f32 v[56:57], v[56:57], v[56:57]
	v_cvt_pk_bf16_f32 v58, v60, v61
	v_cvt_pk_bf16_f32 v59, v62, v63
	v_lshlrev_b64 v[62:63], 7, v[64:65]
	v_cvt_pk_bf16_f32 v60, v56, v57
	v_lshl_add_u64 v[56:57], v[62:63], 0, v[136:137]
	v_lshlrev_b64 v[56:57], 15, v[56:57]
	v_pk_fma_f32 v[52:53], v[52:53], v[172:173], v[112:113] op_sel_hi:[1,0,1]
	v_pk_fma_f32 v[48:49], v[48:49], v[172:173], v[108:109] op_sel_hi:[1,0,1]
	v_lshl_add_u64 v[56:57], s[22:23], 0, v[56:57]
	v_lshl_or_b32 v212, v67, 10, v161
	v_pk_fma_f32 v[54:55], v[54:55], v[172:173], v[114:115] op_sel_hi:[1,0,1]
	v_pk_fma_f32 v[50:51], v[50:51], v[172:173], v[110:111] op_sel_hi:[1,0,1]
	v_max_f32_e32 v53, 0, v53
	v_max_f32_e32 v52, 0, v52
	v_max_f32_e32 v49, 0, v49
	v_max_f32_e32 v48, 0, v48
	v_lshl_add_u64 v[64:65], v[56:57], 0, v[212:213]
	v_max_f32_e32 v55, 0, v55
	v_max_f32_e32 v54, 0, v54
	v_max_f32_e32 v51, 0, v51
	v_max_f32_e32 v50, 0, v50
	v_pk_mul_f32 v[52:53], v[52:53], v[52:53]
	v_pk_mul_f32 v[48:49], v[48:49], v[48:49]
	v_cvt_pk_bf16_f32 v61, v68, v69
	global_store_dwordx4 v[64:65], v[58:61], off nt
	v_pk_mul_f32 v[54:55], v[54:55], v[54:55]
	s_nop 0
	v_pk_mul_f32 v[58:59], v[50:51], v[50:51]
	v_cvt_pk_bf16_f32 v50, v52, v53
	v_cvt_pk_bf16_f32 v51, v54, v55
	v_cvt_pk_bf16_f32 v52, v48, v49
	v_lshl_add_u64 v[48:49], v[62:63], 0, v[128:129]
	v_lshlrev_b64 v[48:49], 15, v[48:49]
	v_lshl_add_u64 v[48:49], s[22:23], 0, v[48:49]
	v_lshl_add_u64 v[54:55], v[48:49], 0, v[212:213]
	v_cvt_pk_bf16_f32 v53, v58, v59
	global_store_dwordx4 v[54:55], v[50:53], off nt
	s_nop 0
	s_nop 0
	v_pk_fma_f32 v[46:47], v[46:47], v[174:175], v[126:127] op_sel_hi:[1,0,1]
	v_pk_fma_f32 v[44:45], v[44:45], v[174:175], v[124:125] op_sel_hi:[1,0,1]
	v_pk_fma_f32 v[42:43], v[42:43], v[174:175], v[122:123] op_sel_hi:[1,0,1]
	v_pk_fma_f32 v[40:41], v[40:41], v[174:175], v[120:121] op_sel_hi:[1,0,1]
	v_max_f32_e32 v45, 0, v45
	v_max_f32_e32 v44, 0, v44
	v_max_f32_e32 v47, 0, v47
	v_max_f32_e32 v46, 0, v46
	v_max_f32_e32 v41, 0, v41
	v_max_f32_e32 v40, 0, v40
	v_max_f32_e32 v43, 0, v43
	v_max_f32_e32 v42, 0, v42
	v_pk_fma_f32 v[36:37], v[36:37], v[174:175], v[112:113] op_sel_hi:[1,0,1]
	v_pk_fma_f32 v[34:35], v[34:35], v[174:175], v[110:111] op_sel_hi:[1,0,1]
	v_pk_fma_f32 v[32:33], v[32:33], v[174:175], v[108:109] op_sel_hi:[1,0,1]
	v_pk_mul_f32 v[46:47], v[46:47], v[46:47]
	v_pk_mul_f32 v[44:45], v[44:45], v[44:45]
	v_pk_mul_f32 v[52:53], v[42:43], v[42:43]
	v_pk_mul_f32 v[42:43], v[40:41], v[40:41]
	v_cvt_pk_bf16_f32 v40, v44, v45
	v_cvt_pk_bf16_f32 v41, v46, v47
	v_pk_fma_f32 v[38:39], v[38:39], v[174:175], v[114:115] op_sel_hi:[1,0,1]
	v_max_f32_e32 v37, 0, v37
	v_max_f32_e32 v36, 0, v36
	v_max_f32_e32 v33, 0, v33
	v_max_f32_e32 v32, 0, v32
	v_max_f32_e32 v35, 0, v35
	v_max_f32_e32 v34, 0, v34
	v_cvt_pk_bf16_f32 v42, v42, v43
	v_cvt_pk_bf16_f32 v43, v52, v53
	global_store_dwordx4 v[64:65], v[40:43], off offset:2048 nt
	v_max_f32_e32 v39, 0, v39
	v_max_f32_e32 v38, 0, v38
	v_pk_mul_f32 v[36:37], v[36:37], v[36:37]
	v_pk_mul_f32 v[40:41], v[34:35], v[34:35]
	v_pk_mul_f32 v[34:35], v[32:33], v[32:33]
	v_cvt_pk_bf16_f32 v32, v36, v37
	v_pk_mul_f32 v[38:39], v[38:39], v[38:39]
	s_nop 0
	v_cvt_pk_bf16_f32 v33, v38, v39
	v_cvt_pk_bf16_f32 v34, v34, v35
	v_cvt_pk_bf16_f32 v35, v40, v41
	global_store_dwordx4 v[54:55], v[32:35], off offset:2048 nt
	s_nop 0
	s_nop 0
	v_pk_fma_f32 v[28:29], v[28:29], v[176:177], v[124:125] op_sel_hi:[1,0,1]
	v_pk_fma_f32 v[30:31], v[30:31], v[176:177], v[126:127] op_sel_hi:[1,0,1]
	v_pk_fma_f32 v[26:27], v[26:27], v[176:177], v[122:123] op_sel_hi:[1,0,1]
	v_pk_fma_f32 v[24:25], v[24:25], v[176:177], v[120:121] op_sel_hi:[1,0,1]
	v_max_f32_e32 v29, 0, v29
	v_max_f32_e32 v28, 0, v28
	v_max_f32_e32 v31, 0, v31
	v_max_f32_e32 v30, 0, v30
	v_max_f32_e32 v25, 0, v25
	v_max_f32_e32 v24, 0, v24
	v_max_f32_e32 v27, 0, v27
	v_max_f32_e32 v26, 0, v26
	v_pk_mul_f32 v[28:29], v[28:29], v[28:29]
	v_pk_fma_f32 v[20:21], v[20:21], v[176:177], v[112:113] op_sel_hi:[1,0,1]
	v_pk_mul_f32 v[30:31], v[30:31], v[30:31]
	v_pk_mul_f32 v[34:35], v[26:27], v[26:27]
	v_pk_mul_f32 v[26:27], v[24:25], v[24:25]
	v_cvt_pk_bf16_f32 v24, v28, v29
	v_or_b32_e32 v28, 0x1000, v212
	v_mov_b32_e32 v29, v213
	v_pk_fma_f32 v[18:19], v[18:19], v[176:177], v[110:111] op_sel_hi:[1,0,1]
	v_pk_fma_f32 v[16:17], v[16:17], v[176:177], v[108:109] op_sel_hi:[1,0,1]
	v_max_f32_e32 v21, 0, v21
	v_max_f32_e32 v20, 0, v20
	v_cvt_pk_bf16_f32 v25, v30, v31
	v_lshl_add_u64 v[30:31], v[56:57], 0, v[28:29]
	v_pk_fma_f32 v[22:23], v[22:23], v[176:177], v[114:115] op_sel_hi:[1,0,1]
	v_max_f32_e32 v17, 0, v17
	v_max_f32_e32 v16, 0, v16
	v_max_f32_e32 v19, 0, v19
	v_max_f32_e32 v18, 0, v18
	v_pk_mul_f32 v[20:21], v[20:21], v[20:21]
	v_cvt_pk_bf16_f32 v26, v26, v27
	v_cvt_pk_bf16_f32 v27, v34, v35
	global_store_dwordx4 v[30:31], v[24:27], off nt
	v_max_f32_e32 v23, 0, v23
	v_max_f32_e32 v22, 0, v22
	v_pk_mul_f32 v[24:25], v[18:19], v[18:19]
	v_pk_mul_f32 v[18:19], v[16:17], v[16:17]
	v_cvt_pk_bf16_f32 v16, v20, v21
	v_lshl_add_u64 v[20:21], v[48:49], 0, v[28:29]
	v_pk_mul_f32 v[22:23], v[22:23], v[22:23]
	v_or_b32_e32 v212, 0x1800, v212
	v_cvt_pk_bf16_f32 v17, v22, v23
	v_cvt_pk_bf16_f32 v18, v18, v19
	v_cvt_pk_bf16_f32 v19, v24, v25
	global_store_dwordx4 v[20:21], v[16:19], off nt
	s_nop 0
	s_nop 0
	v_pk_fma_f32 v[12:13], v[12:13], v[178:179], v[124:125] op_sel_hi:[1,0,1]
	v_pk_fma_f32 v[14:15], v[14:15], v[178:179], v[126:127] op_sel_hi:[1,0,1]
	v_pk_fma_f32 v[10:11], v[10:11], v[178:179], v[122:123] op_sel_hi:[1,0,1]
	v_pk_fma_f32 v[8:9], v[8:9], v[178:179], v[120:121] op_sel_hi:[1,0,1]
	v_max_f32_e32 v13, 0, v13
	v_max_f32_e32 v12, 0, v12
	v_pk_fma_f32 v[4:5], v[4:5], v[178:179], v[112:113] op_sel_hi:[1,0,1]
	v_max_f32_e32 v15, 0, v15
	v_max_f32_e32 v14, 0, v14
	v_max_f32_e32 v9, 0, v9
	v_max_f32_e32 v8, 0, v8
	v_max_f32_e32 v11, 0, v11
	v_max_f32_e32 v10, 0, v10
	v_pk_mul_f32 v[12:13], v[12:13], v[12:13]
	v_pk_fma_f32 v[2:3], v[2:3], v[178:179], v[110:111] op_sel_hi:[1,0,1]
	v_pk_fma_f32 v[0:1], v[0:1], v[178:179], v[108:109] op_sel_hi:[1,0,1]
	v_max_f32_e32 v5, 0, v5
	v_max_f32_e32 v4, 0, v4
	v_pk_mul_f32 v[14:15], v[14:15], v[14:15]
	v_pk_mul_f32 v[18:19], v[10:11], v[10:11]
	v_pk_mul_f32 v[10:11], v[8:9], v[8:9]
	v_cvt_pk_bf16_f32 v8, v12, v13
	v_cvt_pk_bf16_f32 v9, v14, v15
	v_lshl_add_u64 v[12:13], v[56:57], 0, v[212:213]
	v_pk_fma_f32 v[6:7], v[6:7], v[178:179], v[114:115] op_sel_hi:[1,0,1]
	v_max_f32_e32 v1, 0, v1
	v_max_f32_e32 v0, 0, v0
	v_max_f32_e32 v3, 0, v3
	v_max_f32_e32 v2, 0, v2
	v_pk_mul_f32 v[4:5], v[4:5], v[4:5]
	v_cvt_pk_bf16_f32 v10, v10, v11
	v_cvt_pk_bf16_f32 v11, v18, v19
	global_store_dwordx4 v[12:13], v[8:11], off nt
	v_max_f32_e32 v7, 0, v7
	v_max_f32_e32 v6, 0, v6
	v_pk_mul_f32 v[8:9], v[2:3], v[2:3]
	v_pk_mul_f32 v[2:3], v[0:1], v[0:1]
	v_cvt_pk_bf16_f32 v0, v4, v5
	v_lshl_add_u64 v[4:5], v[48:49], 0, v[212:213]
	v_pk_mul_f32 v[6:7], v[6:7], v[6:7]
	s_nop 0
	v_cvt_pk_bf16_f32 v1, v6, v7
	v_cvt_pk_bf16_f32 v2, v2, v3
	v_cvt_pk_bf16_f32 v3, v8, v9
	global_store_dwordx4 v[4:5], v[0:3], off nt
	s_cbranch_vccnz .LBB0_1165
	s_andn2_b64 vcc, exec, s[20:21]
	s_cbranch_vccnz .LBB0_1164
	s_barrier
	s_branch .LBB0_1164
